# v60 with the deferred tile computed AFTER the P2 units on WGs>=128 (tile last instead of tile first)
# baseline (speedup 1.0000x reference)
; #define SEAM(k) do { if (IN(k) && IN((k) + 1)) xcd_barrier(bar); } while (0)
; #define REP(k) for (int rep_ = reframe(F); rep_ < (((MK_DUP) >> (k)) & 1) + 1; ++rep_)
; #define REPBAR(k) do { if ((((MK_DUP) >> (k)) & 1) && rep_ == 0) xcd_barrier(bar); } while (0)
; __global__ void __launch_bounds__(NTHREADS, 2) mk_fwd(Args args) {
;     ...
;     if (IN(2)) REP(2) {
;         if (MK_NSCAN == 0) for (int u = blockIdx.x; u < 1024; u += F.G) spatial_unit(F, args, u >> 3, u & 7);
;         for (int u = blockIdx.x; u < 1024; u += F.G) kv_unit(F, args, u >> 3, u & 7);
;         REPBAR(2);
;     } SEAM(2);
.LBB0_282:
	s_cmp_eq_u32 s101, 1
	s_cbranch_scc0 .Ldefer_norm
	s_mov_b32 s101, 2
	s_mov_b32 s92, s98
	s_mov_b32 s93, 0
	s_branch .Lp2_tail

; #define LAS __attribute__((address_space(3)))
; __device__ __forceinline__ unsigned cvt_pk_bf16(float lo, float hi) { f32x2 v = {lo, hi}; bf16x2_t b = __builtin_convertvector(v, bf16x2_t); return __builtin_bit_cast(unsigned, b); }
; #define REP(k) for (int rep_ = reframe(F); rep_ < (((MK_DUP) >> (k)) & 1) + 1; ++rep_)
; __device__ __forceinline__ void spatial_unit(Frame& F, const Args& a, int n, int g) {
;     LAS unsigned char* Wimg = F.lds; LAS unsigned char* Vimg = F.lds + 32768; LAS float* stats = (LAS float*)(F.lds + 65536);
;     const int t0 = n * 128, ch0 = g * 128, tid = F.tid, lane = F.lane, w = F.wave;
;     const bf16_t* V = (const bf16_t*)(F.ws + WS_V); const bf16_t* U = (const bf16_t*)(F.ws + WS_U); bf16_t* SG = (bf16_t*)(F.ws + WS_SG);
;     const float* vstat = (const float*)(F.ws + WS_VSTAT);
;     if (tid < 128) { const f32x4* p = (const f32x4*)(vstat + (size_t)(t0 + tid) * 32); float s = 0.f, q = 0.f;
; #pragma unroll
;         for (int j = 0; j < 8; ++j) { const f32x4 v = p[j]; s += v[0] + v[2]; q += v[1] + v[3]; }
;         const float mean = s * (1.f / GW), var = q * (1.f / GW) - mean * mean;
;         stats[2 * tid] = mean; stats[2 * tid + 1] = 1.0f / sqrtf(fmaxf(var, 0.f) + EPS); }
;     const float* ws_g = a.in[5] + (size_t)g * 128 * 128;
; #pragma unroll
;     for (int i = 0; i < 4; ++i) { const int id = tid + 512 * i, t = id >> 4, ch = id & 15;
;         const f32x4 x0 = *(const f32x4*)(ws_g + t * 128 + 8 * ch), x1 = *(const f32x4*)(ws_g + t * 128 + 8 * ch + 4);
;         float v[8] = {x0[0], x0[1], x0[2], x0[3], x1[0], x1[1], x1[2], x1[3]};
; #pragma unroll
;         for (int j = 0; j < 8; ++j) v[j] = (8 * ch + j <= t) ? v[j] : 0.f;
;         u32x4 o; o.x = cvt_pk_bf16(v[0], v[1]); o.y = cvt_pk_bf16(v[2], v[3]); o.z = cvt_pk_bf16(v[4], v[5]); o.w = cvt_pk_bf16(v[6], v[7]);
;         *(LAS u32x4*)(Wimg + off_b(t, ch)) = o; }
; __global__ void __launch_bounds__(NTHREADS, 2) mk_fwd(Args args) {
;     ...
;     if (IN(2)) REP(2) {
;         if (MK_NSCAN == 0) for (int u = blockIdx.x; u < 1024; u += F.G) spatial_unit(F, args, u >> 3, u & 7);
.LBB0_336:
	s_cmp_lt_i32 s88, 3
	s_cselect_b64 s[4:5], -1, 0
	s_and_b64 s[4:5], s[4:5], s[0:1]
	s_andn2_b64 vcc, exec, s[4:5]
	v_writelane_b32 v254, s88, 8
	s_nop 1
	v_writelane_b32 v254, s89, 9
	s_cbranch_vccnz .LBB0_353
	s_waitcnt vmcnt(0)
	v_mov_b32_e32 v67, v0
	s_cmpk_gt_i32 s92, 0x3ff
	v_readfirstlane_b32 s0, v67
	s_cbranch_scc1 .LBB0_353
	v_ashrrev_i32_e32 v1, 4, v67
	v_lshlrev_b32_e32 v14, 2, v1
	v_and_b32_e32 v68, 15, v67
	v_and_b32_e32 v14, 12, v14
	v_bfe_u32 v78, v1, 2, 2
	v_bitop3_b32 v14, v14, v68, v78 bitop3:0x36
	v_lshl_add_u32 v81, v14, 4, 0
	v_add_u32_e32 v14, 0x200, v67
	v_ashrrev_i32_e32 v69, 4, v14
	v_lshlrev_b32_e32 v15, 2, v69
	v_and_b32_e32 v15, 12, v15
	v_bfe_u32 v16, v69, 2, 2
	v_bitop3_b32 v15, v15, v68, v16 bitop3:0x36
	v_add_u32_e32 v16, 0x400, v67
	v_ashrrev_i32_e32 v73, 4, v16
	v_lshlrev_b32_e32 v17, 2, v73
	s_load_dwordx8 s[72:79], s[96:97], 0x18
	v_and_b32_e32 v17, 12, v17
	v_bfe_u32 v18, v73, 2, 2
	v_bitop3_b32 v17, v17, v68, v18 bitop3:0x36
	v_add_u32_e32 v18, 0x600, v67
	v_lshlrev_b32_e32 v6, 3, v68
	v_ashrrev_i32_e32 v76, 4, v18
	v_mov_b32_e32 v2, 0
	v_cmp_gt_i32_e64 s[8:9], v6, v1
	v_cmp_lt_i32_e64 s[10:11], v6, v1
	v_or_b32_e32 v7, 2, v6
	v_or_b32_e32 v8, 3, v6
	v_or_b32_e32 v9, 4, v6
	v_or_b32_e32 v10, 5, v6
	v_or_b32_e32 v11, 6, v6
	v_or_b32_e32 v12, 7, v6
	v_cmp_gt_i32_e64 s[24:25], v6, v69
	v_cmp_lt_i32_e64 s[26:27], v6, v69
	v_cmp_gt_i32_e64 s[42:43], v6, v73
	v_cmp_lt_i32_e64 s[44:45], v6, v73
	v_cmp_gt_i32_e64 s[58:59], v6, v76
	v_cmp_lt_i32_e64 s[60:61], v6, v76
	v_lshlrev_b32_e32 v6, 2, v76
	s_waitcnt lgkmcnt(0)
; __device__ __forceinline__ void spatial_unit(Frame& F, const Args& a, int n, int g) {
;     LAS unsigned char* Wimg = F.lds; LAS unsigned char* Vimg = F.lds + 32768; LAS float* stats = (LAS float*)(F.lds + 65536);
;     const int t0 = n * 128, ch0 = g * 128, tid = F.tid, lane = F.lane, w = F.wave;
;     const bf16_t* V = (const bf16_t*)(F.ws + WS_V); const bf16_t* U = (const bf16_t*)(F.ws + WS_U); bf16_t* SG = (bf16_t*)(F.ws + WS_SG);
;     const float* vstat = (const float*)(F.ws + WS_VSTAT);
;     if (tid < 128) { const f32x4* p = (const f32x4*)(vstat + (size_t)(t0 + tid) * 32); float s = 0.f, q = 0.f;
; #pragma unroll
;         for (int j = 0; j < 8; ++j) { const f32x4 v = p[j]; s += v[0] + v[2]; q += v[1] + v[3]; }
;         const float mean = s * (1.f / GW), var = q * (1.f / GW) - mean * mean;
;         stats[2 * tid] = mean; stats[2 * tid + 1] = 1.0f / sqrtf(fmaxf(var, 0.f) + EPS); }
;     const float* ws_g = a.in[5] + (size_t)g * 128 * 128;
; #pragma unroll
;     for (int i = 0; i < 4; ++i) { const int id = tid + 512 * i, t = id >> 4, ch = id & 15;
;         const f32x4 x0 = *(const f32x4*)(ws_g + t * 128 + 8 * ch), x1 = *(const f32x4*)(ws_g + t * 128 + 8 * ch + 4);
;         float v[8] = {x0[0], x0[1], x0[2], x0[3], x1[0], x1[1], x1[2], x1[3]};
; #pragma unroll
;         for (int j = 0; j < 8; ++j) v[j] = (8 * ch + j <= t) ? v[j] : 0.f;
;         u32x4 o; o.x = cvt_pk_bf16(v[0], v[1]); o.y = cvt_pk_bf16(v[2], v[3]); o.z = cvt_pk_bf16(v[4], v[5]); o.w = cvt_pk_bf16(v[6], v[7]);
;         *(LAS u32x4*)(Wimg + off_b(t, ch)) = o; }
;     __syncthreads();
;     const float* lng = a.in[3]; const float* lnb = a.in[4];
;     {
;         u32x4 xv[4]; const int ch = tid & 15;
; #pragma unroll
;         for (int i = 0; i < 4; ++i) xv[i] = __builtin_nontemporal_load((const u32x4*)(V + (size_t)(t0 + (tid >> 4) + 32 * i) * GW + ch0 + 8 * ch));
;         const f32x4 g0 = *(const f32x4*)(lng + ch0 + 8 * ch), g1 = *(const f32x4*)(lng + ch0 + 8 * ch + 4), b0 = *(const f32x4*)(lnb + ch0 + 8 * ch), b1 = *(const f32x4*)(lnb + ch0 + 8 * ch + 4);
; #pragma unroll
;         for (int i = 0; i < 4; ++i) { const int s = (tid >> 4) + 32 * i; const u32x4 x = xv[i];
;             const float mean = stats[2 * s], rstd = stats[2 * s + 1];
;             float v[8] = {bf_lo(x.x), bf_hi(x.x), bf_lo(x.y), bf_hi(x.y), bf_lo(x.z), bf_hi(x.z), bf_lo(x.w), bf_hi(x.w)};
; #pragma unroll
	v_lshlrev_b32_e32 v4, 5, v68
	v_mov_b32_e32 v5, v2
	v_cmp_gt_i32_e64 s[12:13], v7, v1
	v_cmp_gt_i32_e64 s[28:29], v7, v69
	v_cmp_gt_i32_e64 s[46:47], v7, v73
	v_cmp_gt_i32_e64 s[62:63], v7, v76
	v_and_b32_e32 v6, 12, v6
	v_bfe_u32 v7, v76, 2, 2
	v_and_b32_e32 v3, 63, v67
	v_lshl_add_u64 v[46:47], s[76:77], 0, v[4:5]
	v_cmp_gt_i32_e64 s[18:19], v10, v1
	v_cmp_gt_i32_e64 s[36:37], v10, v69
	v_cmp_gt_i32_e64 s[52:53], v10, v73
	v_cmp_gt_i32_e64 s[68:69], v10, v76
	v_bitop3_b32 v6, v6, v68, v7 bitop3:0x36
	v_lshlrev_b32_e32 v44, 4, v68
	v_mov_b32_e32 v45, v2
	v_lshl_add_u64 v[50:51], s[72:73], 0, v[4:5]
	v_lshl_add_u64 v[52:53], s[74:75], 0, v[4:5]
	v_bfe_u32 v5, v67, 2, 2
	v_bfe_u32 v10, v67, 1, 5
	v_lshlrev_b32_e32 v77, 3, v67
	v_cmp_gt_i32_e64 s[16:17], v9, v1
	v_cmp_gt_i32_e64 s[34:35], v9, v69
	v_cmp_gt_i32_e64 s[50:51], v9, v73
	v_cmp_gt_i32_e64 s[66:67], v9, v76
	v_lshl_add_u32 v9, v6, 4, 0
	v_lshl_add_u64 v[6:7], s[94:95], 0, v[44:45]
	v_and_b32_e32 v10, 24, v10
	v_bfe_u32 v45, v3, 1, 1
	v_lshlrev_b32_e32 v3, 2, v5
	v_lshrrev_b32_e32 v19, 3, v67
	v_or_b32_e32 v18, v10, v5
	v_and_or_b32 v79, v19, 2, v3
	v_and_b32_e32 v19, 8, v77
	v_or_b32_e32 v10, 4, v10
	v_lshl_or_b32 v72, v18, 8, v19
	v_or_b32_e32 v18, v10, v5
	v_bfe_u32 v10, v10, 2, 2
	v_lshl_or_b32 v75, v18, 8, v19
	v_or_b32_e32 v18, v79, v45
	v_lshl_or_b32 v89, v18, 4, v72
	v_bitop3_b32 v18, v10, v45, v3 bitop3:0x36
	v_lshl_or_b32 v90, v18, 4, v75
	v_or_b32_e32 v18, 2, v45
	v_bitop3_b32 v18, v10, v18, v3 bitop3:0x36
	v_lshl_or_b32 v92, v18, 4, v75
	v_or_b32_e32 v18, 4, v45
	v_bitop3_b32 v18, v10, v18, v3 bitop3:0x36
	v_lshl_or_b32 v94, v18, 4, v75
	v_or_b32_e32 v18, 6, v45
	v_bitop3_b32 v18, v10, v18, v3 bitop3:0x36
	v_lshl_or_b32 v96, v18, 4, v75
	v_or_b32_e32 v18, 8, v45
	v_bitop3_b32 v18, v10, v18, v3 bitop3:0x36
	s_ashr_i32 s3, s0, 6
	v_bitop3_b32 v19, v45, v79, 2 bitop3:0x36
	v_lshl_or_b32 v98, v18, 4, v75
	v_or_b32_e32 v18, 10, v45
	s_movk_i32 s1, 0x80
	s_add_u32 s80, s94, 0x50600000
	v_lshl_or_b32 v91, v19, 4, v72
	v_bitop3_b32 v19, v45, v79, 4 bitop3:0x36
	v_bitop3_b32 v18, v10, v18, v3 bitop3:0x36
	v_cmp_gt_i32_e64 s[6:7], s1, v67
	s_addc_u32 s81, s95, 0
	v_lshl_or_b32 v93, v19, 4, v72
	v_bitop3_b32 v19, v45, v79, 6 bitop3:0x36
	v_lshl_or_b32 v100, v18, 4, v75
	v_or_b32_e32 v18, 12, v45
	s_lshl_b32 s1, s3, 12
	v_lshl_or_b32 v95, v19, 4, v72
	v_bitop3_b32 v19, v45, v79, 8 bitop3:0x36
	v_bitop3_b32 v18, v10, v18, v3 bitop3:0x36
	s_ashr_i32 s0, s0, 7
	s_add_i32 s1, s1, 0
	v_lshl_or_b32 v97, v19, 4, v72
	v_bitop3_b32 v19, v45, v79, 10 bitop3:0x36
	v_lshl_or_b32 v102, v18, 4, v75
	v_or_b32_e32 v18, 14, v45
	s_cmp_gt_i32 s0, -1
	v_or_b32_e32 v80, v10, v3
	v_lshl_or_b32 v99, v19, 4, v72
	v_bitop3_b32 v19, v45, v79, 12 bitop3:0x36
	v_bitop3_b32 v3, v10, v18, v3 bitop3:0x36
	v_lshlrev_b32_e32 v10, 2, v67
	s_cselect_b64 s[74:75], -1, 0
	s_cmp_gt_i32 s0, 0
	v_lshl_or_b32 v101, v19, 4, v72
	v_bitop3_b32 v19, v45, v79, 14 bitop3:0x36
	v_lshl_or_b32 v104, v3, 4, v75
	v_bfe_u32 v3, v67, 4, 2
	v_and_b32_e32 v10, 12, v10
	s_cselect_b64 s[82:83], -1, 0
	s_cmp_gt_i32 s0, 1
	s_mov_b64 s[70:71], 0x3a600000
	v_lshl_or_b32 v103, v19, 4, v72
	v_lshl_add_u32 v18, v68, 8, s1
	v_bitop3_b32 v19, v10, v3, v5 bitop3:0x36
	v_or_b32_e32 v20, 4, v3
	s_cselect_b64 s[84:85], -1, 0
	v_or_b32_e32 v21, 8, v3
	s_cmp_gt_i32 s0, 2
	v_or_b32_e32 v3, 12, v3
	v_lshl_or_b32 v105, s3, 4, v68
	s_movk_i32 s33, 0x210
	s_mov_b64 s[0:1], 0x38600000
	v_writelane_b32 v254, s4, 10
	v_lshl_add_u64 v[48:49], v[6:7], 0, s[70:71]
	v_bitop3_b32 v20, v10, v20, v5 bitop3:0x36
	v_bitop3_b32 v21, v10, v21, v5 bitop3:0x36
	s_cselect_b64 s[86:87], -1, 0
	v_bitop3_b32 v3, v10, v3, v5 bitop3:0x36
	v_mul_lo_u32 v5, v105, s33
	s_add_i32 s70, 0, 0x10400
	v_lshl_add_u64 v[54:55], v[6:7], 0, s[0:1]
	s_mov_b64 s[0:1], 0x51000000
	v_writelane_b32 v254, s5, 11
	v_lshlrev_b32_e32 v36, 7, v1
	v_cmp_gt_i32_e64 s[14:15], v8, v1
	v_lshlrev_b32_e32 v13, 8, v1
	v_lshlrev_b32_e32 v38, 7, v69
	v_cmp_gt_i32_e64 s[30:31], v8, v69
	v_lshlrev_b32_e32 v14, 8, v69
	v_lshl_add_u32 v15, v15, 4, 0
	v_lshlrev_b32_e32 v40, 7, v73
	v_cmp_gt_i32_e64 s[48:49], v8, v73
	v_lshlrev_b32_e32 v16, 8, v73
	v_lshl_add_u32 v17, v17, 4, 0
	v_lshlrev_b32_e32 v42, 7, v76
	v_cmp_gt_i32_e64 s[64:65], v8, v76
	v_lshlrev_b32_e32 v8, 8, v76
	v_add_u32_e32 v84, 32, v1
	v_add_u32_e32 v83, 64, v1
	v_add_u32_e32 v82, 0x60, v1
	v_lshlrev_b32_e32 v19, 4, v19
	v_lshlrev_b32_e32 v20, 4, v20
	v_lshlrev_b32_e32 v21, 4, v21
	v_lshlrev_b32_e32 v3, 4, v3
	v_add_u32_e32 v5, s70, v5
	v_and_b32_e32 v10, 48, v67
	v_add_u32_e32 v4, s70, v4
	v_lshl_add_u64 v[56:57], v[6:7], 0, s[0:1]
	v_mul_lo_u32 v6, v1, s33
	s_lshl_b32 s33, s92, 4
	s_mov_b32 s0, s92
	v_ashrrev_i32_e32 v37, 31, v36
	v_cmp_gt_i32_e64 s[20:21], v11, v1
	v_cmp_gt_i32_e64 s[22:23], v12, v1
	s_mov_b32 s77, 0
	v_ashrrev_i32_e32 v39, 31, v38
	v_cmp_gt_i32_e64 s[38:39], v11, v69
	v_cmp_gt_i32_e64 s[40:41], v12, v69
	v_ashrrev_i32_e32 v41, 31, v40
	v_cmp_gt_i32_e64 s[54:55], v11, v73
	v_cmp_gt_i32_e64 s[56:57], v12, v73
	v_ashrrev_i32_e32 v43, 31, v42
	v_lshlrev_b32_e32 v85, 3, v1
	v_lshlrev_b32_e32 v86, 3, v84
	v_lshlrev_b32_e32 v70, 8, v84
	v_lshlrev_b32_e32 v87, 3, v83
	v_lshlrev_b32_e32 v71, 8, v83
	v_lshlrev_b32_e32 v88, 3, v82
	v_lshlrev_b32_e32 v74, 8, v82
	s_movk_i32 s4, 0x80
	s_movk_i32 s90, 0x800
	v_mov_b32_e32 v106, 0x260
	v_add_u32_e32 v107, v15, v14
	v_add_u32_e32 v108, v17, v16
	v_add_u32_e32 v109, v9, v8
	v_add_u32_e32 v110, v18, v19
	v_add_u32_e32 v111, v18, v20
	v_add_u32_e32 v112, v18, v21
	v_add_u32_e32 v113, v18, v3
	v_add_u32_e32 v114, v5, v10
	v_add_u32_e32 v115, v4, v6
	v_add_u32_e32 v66, v81, v13
	s_mov_b32 s91, s33
	v_writelane_b32 v254, s0, 12
	v_cmp_gt_i32_e64 s[70:71], v11, v76
	v_cmp_gt_i32_e64 s[72:73], v12, v76
	v_writelane_b32 v254, s1, 13
	s_movk_i32 s100, 0x380
	s_cmpk_lt_i32 s92, 0x80
	s_cbranch_scc1 .Lp2_sp_go
	s_movk_i32 s100, 0x400
	s_addk_i32 s92, 0x300
	s_lshl_b32 s91, s92, 4

; #define SEAM(k) do { if (IN(k) && IN((k) + 1)) xcd_barrier(bar); } while (0)
; __device__ __forceinline__ void xcd_barrier(const XcdBarrier& b) {
;     asm volatile("s_waitcnt vmcnt(0)" ::: "memory");
;     __syncthreads();
;     if (threadIdx.x == 0) {
;         unsigned* bar = b.bar;
;         __builtin_amdgcn_s_waitcnt(0);
;         unsigned nloc = b.st[0], nx = b.st[1];
;         if (nloc == 0u) { xcd_barrier_complete(bar, b.x, nloc, nx); b.st[0] = nloc; b.st[1] = nx; }
; __global__ void __launch_bounds__(NTHREADS, 2) mk_fwd(Args args) {
;     ...
;     } SEAM(2);
.Lp2_tail:
	v_readlane_b32 s92, v254, 12
	s_load_dwordx2 s[88:89], s[96:97], 0xc0
	s_movk_i32 s2, 0x100
	v_readlane_b32 s4, v254, 10
	v_readlane_b32 s5, v254, 11
	s_cmp_lg_u32 s101, 0
	s_cbranch_scc1 .Lp2_done
	s_cmpk_lt_i32 s92, 0x80
	s_cbranch_scc1 .Lp2_done
	s_waitcnt vmcnt(0) lgkmcnt(0)
	s_add_i32 s92, s92, 0xb00
	s_movk_i32 s3, 128
	s_movk_i32 s99, 0xc00
	s_mov_b32 s101, 1
	s_branch .Lgemm_entry
.Lp2_done:
.LBB0_353:
	s_waitcnt lgkmcnt(0)
	s_cmp_gt_i32 s89, 3
	s_cselect_b64 s[0:1], -1, 0
	s_and_b64 s[4:5], s[4:5], s[0:1]
	s_andn2_b64 vcc, exec, s[4:5]
	s_cbranch_vccnz .LBB0_407
	s_waitcnt vmcnt(0)
	s_barrier
	s_mov_b64 s[4:5], exec
	v_readlane_b32 s6, v254, 6
	v_readlane_b32 s7, v254, 7
	s_and_b64 s[6:7], s[4:5], s[6:7]
	s_mov_b64 exec, s[6:7]
	s_cbranch_execz .LBB0_406
	s_add_i32 s3, 0, 0x23020
	v_mov_b32_e32 v1, s3
	s_waitcnt vmcnt(0) expcnt(0) lgkmcnt(0)
	ds_read_b32 v3, v1
	s_add_i32 s3, 0, 0x23024
	v_mov_b32_e32 v1, s3
	ds_read_b32 v1, v1
	s_waitcnt lgkmcnt(1)
	v_cmp_ne_u32_e32 vcc, 0, v3
	s_cbranch_vccnz .LBB0_370
	v_readlane_b32 s6, v254, 0
	v_readlane_b32 s7, v254, 1
	s_load_dwordx2 s[10:11], s[6:7], 0x4
	s_add_u32 s6, s94, 0x4200
	s_addc_u32 s7, s95, 0
	s_add_u32 s8, s94, 0x4400
	s_addc_u32 s9, s95, 0
	s_waitcnt lgkmcnt(0)
	s_mul_i32 s3, s10, s2
	s_add_u32 s10, s94, 0x4500
	s_mul_i32 s3, s3, s11
	s_addc_u32 s11, s95, 0
	s_add_u32 s12, s94, 0x4600
	s_addc_u32 s13, s95, 0
	s_add_u32 s14, s94, 0x4700
	s_addc_u32 s15, s95, 0
	s_add_u32 s16, s94, 0x4800
	s_addc_u32 s17, s95, 0
	s_add_u32 s18, s94, 0x4900
	s_addc_u32 s19, s95, 0
	s_add_u32 s20, s94, 0x4a00
	s_addc_u32 s21, s95, 0
	s_add_u32 s22, s94, 0x4b00
	s_addc_u32 s23, s95, 0
	s_add_u32 s24, s94, 0x4c00
	s_addc_u32 s25, s95, 0
	s_add_u32 s26, s94, 0x4d00
	s_addc_u32 s27, s95, 0
	s_add_u32 s28, s94, 0x4e00
	s_addc_u32 s29, s95, 0
	s_add_u32 s30, s94, 0x4f00
	s_addc_u32 s31, s95, 0
	s_add_u32 s34, s94, 0x5000
	s_addc_u32 s35, s95, 0
	s_add_u32 s36, s94, 0x5100
	s_addc_u32 s37, s95, 0
	s_add_u32 s38, s94, 0x5200
	s_addc_u32 s39, s95, 0
	s_add_u32 s40, s94, 0x5300
	s_addc_u32 s41, s95, 0
	s_mov_b32 s33, 1
	v_mov_b32_e32 v17, 0
	s_branch .LBB0_358
